# strategy 4: one static s_setprio 1 for waves 4-7 at entry, all 64 per-phase flips in the GEMM loops deleted (on top of v41)
# baseline (speedup 1.0000x reference)
.LBB0_5:
	s_or_b64 exec, exec, s[0:1]
	s_add_i32 s0, 0, 0x25ff0
	v_mov_b32 v0, s0
	ds_read_b32 v0, v0 offset:8
	v_mov_b32 v1, s0
	ds_read_b32 v1, v1 offset:12
	v_writelane_b32 v250, s0, 4
	s_lshr_b32 s43, s28, 6
	s_cmp_ge_u32 s43, 4
	s_cbranch_scc0 .Lprio_done
	s_setprio 1
.Lprio_done:
	s_waitcnt lgkmcnt(1)
	v_readfirstlane_b32 s0, v0
	s_cmp_lt_i32 s0, 1
	s_waitcnt lgkmcnt(0)
	v_readfirstlane_b32 s26, v1
	s_cselect_b64 s[0:1], -1, 0
	s_cmp_gt_i32 s26, 0
	s_cselect_b64 s[2:3], -1, 0
	s_and_b64 s[0:1], s[0:1], s[2:3]
	s_andn2_b64 vcc, exec, s[0:1]
	s_cbranch_vccnz .LBB0_136
	s_cmpk_gt_i32 s94, 0x18df
	v_mbcnt_lo_u32_b32 v74, -1, 0
	v_mbcnt_hi_u32_b32 v74, -1, v74
	v_lshl_add_u32 v64, s43, 6, v74
	s_cbranch_scc1 .LBB0_32
	v_lshlrev_b32_e32 v0, 2, v64
	v_and_b32_e32 v65, 0xfc, v0
	v_ashrrev_i32_e32 v0, 3, v64
	s_movk_i32 s2, 0x110
	v_ashrrev_i32_e32 v76, 4, v64
	v_and_b32_e32 v75, -8, v0
	v_mul_lo_u32 v0, v76, s2
	v_add_u32_e32 v2, 0x200, v64
	v_add_u32_e32 v77, 0, v0
	v_lshlrev_b32_e32 v0, 4, v64
	v_ashrrev_i32_e32 v78, 4, v2
	v_add_u32_e32 v3, 0x400, v64
	v_and_b32_e32 v66, 0xf0, v0
	v_mul_lo_u32 v0, v78, s2
	v_ashrrev_i32_e32 v80, 4, v3
	v_add_u32_e32 v4, 0x600, v64
	v_add_u32_e32 v79, 0, v0
	v_mul_lo_u32 v0, v80, s2
	v_ashrrev_i32_e32 v82, 4, v4
	v_add_u32_e32 v5, 0x800, v64
	v_add_u32_e32 v81, 0, v0
	v_mul_lo_u32 v0, v82, s2
	v_ashrrev_i32_e32 v84, 4, v5
	v_add_u32_e32 v6, 0xa00, v64
	v_add_u32_e32 v83, 0, v0
	v_mul_lo_u32 v0, v84, s2
	v_ashrrev_i32_e32 v86, 4, v6
	v_add_u32_e32 v7, 0xc00, v64
	v_add_u32_e32 v85, 0, v0
	v_mul_lo_u32 v0, v86, s2
	v_ashrrev_i32_e32 v88, 4, v7
	v_add_u32_e32 v87, 0, v0
	v_mul_lo_u32 v0, v88, s2
	v_add_u32_e32 v89, 0, v0
	v_lshlrev_b32_e32 v0, 3, v64
	s_movk_i32 s4, 0x210
	v_and_b32_e32 v0, 0xf8, v0
	v_ashrrev_i32_e32 v93, 5, v2
	v_lshlrev_b32_e32 v11, 1, v0
	v_mul_lo_u32 v2, v93, s4
	v_ashrrev_i32_e32 v95, 5, v3
	v_add3_u32 v94, 0, v2, v11
	v_mul_lo_u32 v2, v95, s4
	v_ashrrev_i32_e32 v97, 5, v4
	v_add3_u32 v96, 0, v2, v11
	v_mul_lo_u32 v2, v97, s4
	v_ashrrev_i32_e32 v99, 5, v5
	v_add3_u32 v98, 0, v2, v11
	v_mul_lo_u32 v2, v99, s4
	v_ashrrev_i32_e32 v101, 5, v6
	v_add_u32_e32 v8, 0xe00, v64
	v_add3_u32 v100, 0, v2, v11
	v_mul_lo_u32 v2, v101, s4
	v_ashrrev_i32_e32 v103, 5, v7
	v_add3_u32 v102, 0, v2, v11
	v_mul_lo_u32 v2, v103, s4
	v_ashrrev_i32_e32 v105, 5, v8
	v_add3_u32 v104, 0, v2, v11
	v_mul_lo_u32 v2, v105, s4
	v_add3_u32 v106, 0, v2, v11
	v_add_u32_e32 v2, 0x1000, v64
	v_ashrrev_i32_e32 v107, 5, v2
	v_mul_lo_u32 v2, v107, s4
	v_add3_u32 v108, 0, v2, v11
	v_add_u32_e32 v2, 0x1200, v64
	v_ashrrev_i32_e32 v109, 5, v2
	v_mul_lo_u32 v2, v109, s4
	v_add3_u32 v110, 0, v2, v11
	v_add_u32_e32 v2, 0x1400, v64
	v_ashrrev_i32_e32 v111, 5, v2
	v_mul_lo_u32 v2, v111, s4
	v_add3_u32 v112, 0, v2, v11
	v_add_u32_e32 v2, 0x1600, v64
	v_ashrrev_i32_e32 v113, 5, v2
	v_mul_lo_u32 v2, v113, s4
	v_add3_u32 v114, 0, v2, v11
	v_add_u32_e32 v2, 0x1800, v64
	v_ashrrev_i32_e32 v115, 5, v2
	v_mul_lo_u32 v2, v115, s4
	v_add3_u32 v116, 0, v2, v11
	v_add_u32_e32 v2, 0x1a00, v64
	v_ashrrev_i32_e32 v117, 5, v2
	v_mul_lo_u32 v2, v117, s4
	s_cmpk_eq_i32 s37, 0x100
	v_add3_u32 v118, 0, v2, v11
	v_add_u32_e32 v2, 0x1c00, v64
	s_cselect_b64 s[0:1], -1, 0
	s_add_u32 s18, s60, 0x21c10000
	v_ashrrev_i32_e32 v119, 5, v2
	s_addc_u32 s19, s61, 0
	v_mul_lo_u32 v2, v119, s4
	s_load_dwordx2 s[6:7], s[70:71], 0x108
	s_load_dwordx2 s[8:9], s[70:71], 0xf8
	s_load_dwordx2 s[10:11], s[70:71], 0xd8
	s_load_dwordx2 s[12:13], s[70:71], 0x38
	v_add3_u32 v120, 0, v2, v11
	v_add_u32_e32 v2, 0x1e00, v64
	s_add_u32 s21, s60, 0x1c10000
	v_ashrrev_i32_e32 v121, 5, v2
	s_addc_u32 s22, s61, 0
	v_mul_lo_u32 v2, v121, s4
	s_add_u32 s23, s60, 0x1410000
	v_ashrrev_i32_e32 v90, 4, v8
	v_lshlrev_b32_e32 v9, 1, v75
	v_ashrrev_i32_e32 v91, 5, v64
	v_add3_u32 v122, 0, v2, v11
	v_mul_u32_u24_e32 v2, 0x210, v65
	s_addc_u32 s24, s61, 0
	v_mul_u32_u24_e32 v1, 0x110, v65
	v_mov_b32_e32 v69, 0
	v_mul_lo_u32 v10, v91, s4
	v_add3_u32 v123, 0, v9, v2
	v_mul_lo_u32 v2, v90, s2
	s_movk_i32 s2, 0x80
	s_add_u32 s25, s60, 0x10000
	s_mov_b32 s3, 0
	v_mov_b32_e32 v67, v69
	s_movk_i32 s20, 0x600
	v_add3_u32 v92, 0, v10, v11
	v_add_u32_e32 v124, 0, v2
	v_cmp_gt_u32_e64 s[4:5], s2, v65
	s_addc_u32 s27, s61, 0
	v_add3_u32 v125, 0, v75, v1
	v_lshlrev_b32_e32 v70, 1, v0
	s_movk_i32 s29, 0x2840
	s_mov_b32 s30, s94
	v_add_u32_e32 v126, 0x380, v65
	s_branch .LBB0_9

.LBB0_538:
	ds_read_b128 v[0:3], v193
	ds_read_b128 v[8:11], v193 offset:2048
	ds_read_b128 v[4:7], v195
	ds_read_b128 v[12:15], v195 offset:2048
	s_add_u32 s15, s24, 0x80
	s_addc_u32 s23, s25, 0
	s_and_b64 s[26:27], s[26:27], exec
	s_cselect_b32 s29, s19, s23
	s_cselect_b32 s28, s18, s15
	s_cselect_b32 s27, s17, s3
	s_cselect_b32 s26, s16, s2
	v_lshl_add_u64 v[16:17], s[24:25], 0, v[168:169]
	s_add_i32 m0, s47, 0xc000
	ds_read_b128 v[218:221], v192
	ds_read_b128 v[226:229], v192 offset:2048
	ds_read_b128 v[222:225], v194
	ds_read_b128 v[230:233], v194 offset:2048
	ds_read_b128 v[234:237], v192 offset:4096
	ds_read_b128 v[242:245], v192 offset:6144
	ds_read_b128 v[238:241], v194 offset:4096
	ds_read_b128 v[246:249], v194 offset:6144
	global_load_lds_dwordx4 v[16:17], off
	v_lshl_add_u64 v[16:17], s[24:25], 0, v[174:175]
	s_add_i32 m0, s47, 0xe000
	s_nop 0
	global_load_lds_dwordx4 v[16:17], off
	s_waitcnt lgkmcnt(8)
	s_barrier
	s_waitcnt lgkmcnt(0)
	s_waitcnt lgkmcnt(0)
	v_mfma_scale_f32_16x16x128_f8f6f4 v[156:159], v[0:7], v[218:225], v[156:159], v191, v191 op_sel_hi:[0,0,0]
	v_mfma_scale_f32_16x16x128_f8f6f4 v[152:155], v[8:15], v[218:225], v[152:155], v191, v191 op_sel_hi:[0,0,0]
	v_mfma_scale_f32_16x16x128_f8f6f4 v[148:151], v[0:7], v[226:233], v[148:151], v191, v191 op_sel_hi:[0,0,0]
	v_mfma_scale_f32_16x16x128_f8f6f4 v[144:147], v[8:15], v[226:233], v[144:147], v191, v191 op_sel_hi:[0,0,0]
	v_mfma_scale_f32_16x16x128_f8f6f4 v[140:143], v[0:7], v[234:241], v[140:143], v191, v191 op_sel_hi:[0,0,0]
	v_mfma_scale_f32_16x16x128_f8f6f4 v[136:139], v[8:15], v[234:241], v[136:139], v191, v191 op_sel_hi:[0,0,0]
	v_mfma_scale_f32_16x16x128_f8f6f4 v[132:135], v[0:7], v[242:249], v[132:135], v191, v191 op_sel_hi:[0,0,0]
	v_mfma_scale_f32_16x16x128_f8f6f4 v[128:131], v[8:15], v[242:249], v[128:131], v191, v191 op_sel_hi:[0,0,0]
	s_barrier
	s_mov_b32 m0, s30
	v_lshl_add_u64 v[182:183], s[26:27], 0, v[162:163]
	ds_read_b128 v[16:19], v193 offset:16384
	ds_read_b128 v[24:27], v193 offset:18432
	ds_read_b128 v[20:23], v195 offset:16384
	ds_read_b128 v[28:31], v195 offset:18432
	global_load_lds_dwordx4 v[182:183], off
	v_lshl_add_u64 v[184:185], s[26:27], 0, v[164:165]
	s_mov_b32 m0, s46
	s_nop 0
	global_load_lds_dwordx4 v[184:185], off
	s_barrier
	s_waitcnt lgkmcnt(0)
	s_waitcnt lgkmcnt(0)
	v_mfma_scale_f32_16x16x128_f8f6f4 v[92:95], v[16:23], v[218:225], v[92:95], v191, v191 op_sel_hi:[0,0,0]
	v_mfma_scale_f32_16x16x128_f8f6f4 v[88:91], v[24:31], v[218:225], v[88:91], v191, v191 op_sel_hi:[0,0,0]
	v_mfma_scale_f32_16x16x128_f8f6f4 v[84:87], v[16:23], v[226:233], v[84:87], v191, v191 op_sel_hi:[0,0,0]
	v_mfma_scale_f32_16x16x128_f8f6f4 v[80:83], v[24:31], v[226:233], v[80:83], v191, v191 op_sel_hi:[0,0,0]
	v_mfma_scale_f32_16x16x128_f8f6f4 v[76:79], v[16:23], v[234:241], v[76:79], v191, v191 op_sel_hi:[0,0,0]
	v_mfma_scale_f32_16x16x128_f8f6f4 v[72:75], v[24:31], v[234:241], v[72:75], v191, v191 op_sel_hi:[0,0,0]
	v_mfma_scale_f32_16x16x128_f8f6f4 v[68:71], v[16:23], v[242:249], v[68:71], v191, v191 op_sel_hi:[0,0,0]
	v_mfma_scale_f32_16x16x128_f8f6f4 v[64:67], v[24:31], v[242:249], v[64:67], v191, v191 op_sel_hi:[0,0,0]
	s_mov_b32 m0, s47
	s_barrier
	ds_read_b128 v[218:221], v192 offset:16384
	ds_read_b128 v[226:229], v192 offset:18432
	ds_read_b128 v[222:225], v194 offset:16384
	ds_read_b128 v[230:233], v194 offset:18432
	ds_read_b128 v[234:237], v192 offset:20480
	ds_read_b128 v[242:245], v192 offset:22528
	ds_read_b128 v[238:241], v194 offset:20480
	ds_read_b128 v[246:249], v194 offset:22528
	global_load_lds_dwordx4 v172, s[28:29]
	s_mov_b32 m0, s83
	v_mov_b32_e32 v187, v173
	global_load_lds_dwordx4 v186, s[28:29]
	s_barrier
	s_waitcnt lgkmcnt(0)
	v_lshl_add_u64 v[188:189], s[28:29], 0, v[172:173]
	v_lshl_add_u64 v[186:187], s[28:29], 0, v[186:187]
	s_waitcnt lgkmcnt(0)
	v_mfma_scale_f32_16x16x128_f8f6f4 v[124:127], v[0:7], v[218:225], v[124:127], v191, v191 op_sel_hi:[0,0,0]
	v_mfma_scale_f32_16x16x128_f8f6f4 v[120:123], v[8:15], v[218:225], v[120:123], v191, v191 op_sel_hi:[0,0,0]
	v_mfma_scale_f32_16x16x128_f8f6f4 v[116:119], v[0:7], v[226:233], v[116:119], v191, v191 op_sel_hi:[0,0,0]
	v_mfma_scale_f32_16x16x128_f8f6f4 v[112:115], v[8:15], v[226:233], v[112:115], v191, v191 op_sel_hi:[0,0,0]
	v_mfma_scale_f32_16x16x128_f8f6f4 v[108:111], v[0:7], v[234:241], v[108:111], v191, v191 op_sel_hi:[0,0,0]
	v_mfma_scale_f32_16x16x128_f8f6f4 v[104:107], v[8:15], v[234:241], v[104:107], v191, v191 op_sel_hi:[0,0,0]
	v_mfma_scale_f32_16x16x128_f8f6f4 v[100:103], v[0:7], v[242:249], v[100:103], v191, v191 op_sel_hi:[0,0,0]
	v_mfma_scale_f32_16x16x128_f8f6f4 v[96:99], v[8:15], v[242:249], v[96:99], v191, v191 op_sel_hi:[0,0,0]
	s_barrier
	s_add_u32 s72, s26, 0x20000
	s_addc_u32 s73, s27, 0
	s_mov_b32 m0, s82
	v_lshl_add_u64 v[0:1], s[72:73], 0, v[162:163]
	global_load_lds_dwordx4 v[0:1], off
	v_lshl_add_u64 v[0:1], s[72:73], 0, v[164:165]
	s_mov_b32 m0, s80
	s_nop 0
	global_load_lds_dwordx4 v[0:1], off
	s_waitcnt vmcnt(6)
	s_barrier
	v_mfma_scale_f32_16x16x128_f8f6f4 v[60:63], v[16:23], v[218:225], v[60:63], v191, v191 op_sel_hi:[0,0,0]
	v_mfma_scale_f32_16x16x128_f8f6f4 v[56:59], v[24:31], v[218:225], v[56:59], v191, v191 op_sel_hi:[0,0,0]
	v_mfma_scale_f32_16x16x128_f8f6f4 v[52:55], v[16:23], v[226:233], v[52:55], v191, v191 op_sel_hi:[0,0,0]
	v_mfma_scale_f32_16x16x128_f8f6f4 v[48:51], v[24:31], v[226:233], v[48:51], v191, v191 op_sel_hi:[0,0,0]
	v_mfma_scale_f32_16x16x128_f8f6f4 v[44:47], v[16:23], v[234:241], v[44:47], v191, v191 op_sel_hi:[0,0,0]
	v_mfma_scale_f32_16x16x128_f8f6f4 v[40:43], v[24:31], v[234:241], v[40:43], v191, v191 op_sel_hi:[0,0,0]
	v_mfma_scale_f32_16x16x128_f8f6f4 v[36:39], v[16:23], v[242:249], v[36:39], v191, v191 op_sel_hi:[0,0,0]
	v_mfma_scale_f32_16x16x128_f8f6f4 v[32:35], v[24:31], v[242:249], v[32:35], v191, v191 op_sel_hi:[0,0,0]
	s_barrier
	ds_read_b128 v[0:3], v193 offset:32768
	ds_read_b128 v[8:11], v193 offset:34816
	ds_read_b128 v[4:7], v195 offset:32768
	ds_read_b128 v[12:15], v195 offset:34816
	s_mov_b32 m0, s81
	v_lshl_add_u64 v[180:181], s[28:29], 0, v[180:181]
	ds_read_b128 v[16:19], v192 offset:32768
	ds_read_b128 v[24:27], v192 offset:34816
	ds_read_b128 v[20:23], v194 offset:32768
	ds_read_b128 v[28:31], v194 offset:34816
	ds_read_b128 v[218:221], v192 offset:36864
	ds_read_b128 v[226:229], v192 offset:38912
	ds_read_b128 v[222:225], v194 offset:36864
	ds_read_b128 v[230:233], v194 offset:38912
	global_load_lds_dwordx4 v[180:181], off
	v_lshl_add_u64 v[178:179], s[28:29], 0, v[178:179]
	s_mov_b32 m0, s50
	s_nop 0
	global_load_lds_dwordx4 v[178:179], off
	s_waitcnt lgkmcnt(8)
	s_barrier
	s_waitcnt lgkmcnt(0)
	s_waitcnt lgkmcnt(0)
	v_mfma_scale_f32_16x16x128_f8f6f4 v[156:159], v[0:7], v[16:23], v[156:159], v191, v191 op_sel_hi:[0,0,0]
	v_mfma_scale_f32_16x16x128_f8f6f4 v[152:155], v[8:15], v[16:23], v[152:155], v191, v191 op_sel_hi:[0,0,0]
	v_mfma_scale_f32_16x16x128_f8f6f4 v[148:151], v[0:7], v[24:31], v[148:151], v191, v191 op_sel_hi:[0,0,0]
	v_mfma_scale_f32_16x16x128_f8f6f4 v[144:147], v[8:15], v[24:31], v[144:147], v191, v191 op_sel_hi:[0,0,0]
	v_mfma_scale_f32_16x16x128_f8f6f4 v[140:143], v[0:7], v[218:225], v[140:143], v191, v191 op_sel_hi:[0,0,0]
	v_mfma_scale_f32_16x16x128_f8f6f4 v[136:139], v[8:15], v[218:225], v[136:139], v191, v191 op_sel_hi:[0,0,0]
	v_mfma_scale_f32_16x16x128_f8f6f4 v[132:135], v[0:7], v[226:233], v[132:135], v191, v191 op_sel_hi:[0,0,0]
	v_mfma_scale_f32_16x16x128_f8f6f4 v[128:131], v[8:15], v[226:233], v[128:131], v191, v191 op_sel_hi:[0,0,0]
	s_barrier
	s_mov_b32 m0, s51
	v_lshl_add_u64 v[178:179], v[182:183], 0, s[40:41]
	ds_read_b128 v[234:237], v193 offset:49152
	ds_read_b128 v[242:245], v193 offset:51200
	ds_read_b128 v[238:241], v195 offset:49152
	ds_read_b128 v[246:249], v195 offset:51200
	global_load_lds_dwordx4 v[178:179], off
	v_lshl_add_u64 v[178:179], v[184:185], 0, s[40:41]
	s_mov_b32 m0, s70
	s_nop 0
	global_load_lds_dwordx4 v[178:179], off
	s_barrier
	s_waitcnt lgkmcnt(0)
	s_waitcnt lgkmcnt(0)
	v_mfma_scale_f32_16x16x128_f8f6f4 v[92:95], v[234:241], v[16:23], v[92:95], v191, v191 op_sel_hi:[0,0,0]
	v_mfma_scale_f32_16x16x128_f8f6f4 v[88:91], v[242:249], v[16:23], v[88:91], v191, v191 op_sel_hi:[0,0,0]
	v_mfma_scale_f32_16x16x128_f8f6f4 v[84:87], v[234:241], v[24:31], v[84:87], v191, v191 op_sel_hi:[0,0,0]
	v_mfma_scale_f32_16x16x128_f8f6f4 v[80:83], v[242:249], v[24:31], v[80:83], v191, v191 op_sel_hi:[0,0,0]
	v_mfma_scale_f32_16x16x128_f8f6f4 v[76:79], v[234:241], v[218:225], v[76:79], v191, v191 op_sel_hi:[0,0,0]
	v_mfma_scale_f32_16x16x128_f8f6f4 v[72:75], v[242:249], v[218:225], v[72:75], v191, v191 op_sel_hi:[0,0,0]
	v_mfma_scale_f32_16x16x128_f8f6f4 v[68:71], v[234:241], v[226:233], v[68:71], v191, v191 op_sel_hi:[0,0,0]
	v_mfma_scale_f32_16x16x128_f8f6f4 v[64:67], v[242:249], v[226:233], v[64:67], v191, v191 op_sel_hi:[0,0,0]
	s_mov_b32 m0, s71
	v_lshl_add_u64 v[188:189], v[188:189], 0, s[40:41]
	s_barrier
	ds_read_b128 v[16:19], v192 offset:49152
	ds_read_b128 v[24:27], v192 offset:51200
	ds_read_b128 v[20:23], v194 offset:49152
	ds_read_b128 v[28:31], v194 offset:51200
	ds_read_b128 v[178:181], v192 offset:53248
	ds_read_b128 v[218:221], v192 offset:55296
	ds_read_b128 v[182:185], v194 offset:53248
	ds_read_b128 v[222:225], v194 offset:55296
	global_load_lds_dwordx4 v[188:189], off
	v_lshl_add_u64 v[186:187], v[186:187], 0, s[40:41]
	s_mov_b32 m0, s87
	s_nop 0
	global_load_lds_dwordx4 v[186:187], off
	s_barrier
	s_waitcnt lgkmcnt(0)
	s_waitcnt lgkmcnt(0)
	v_mfma_scale_f32_16x16x128_f8f6f4 v[124:127], v[0:7], v[16:23], v[124:127], v191, v191 op_sel_hi:[0,0,0]
	v_mfma_scale_f32_16x16x128_f8f6f4 v[120:123], v[8:15], v[16:23], v[120:123], v191, v191 op_sel_hi:[0,0,0]
	v_mfma_scale_f32_16x16x128_f8f6f4 v[116:119], v[0:7], v[24:31], v[116:119], v191, v191 op_sel_hi:[0,0,0]
	v_mfma_scale_f32_16x16x128_f8f6f4 v[112:115], v[8:15], v[24:31], v[112:115], v191, v191 op_sel_hi:[0,0,0]
	v_mfma_scale_f32_16x16x128_f8f6f4 v[108:111], v[0:7], v[178:185], v[108:111], v191, v191 op_sel_hi:[0,0,0]
	v_mfma_scale_f32_16x16x128_f8f6f4 v[104:107], v[8:15], v[178:185], v[104:107], v191, v191 op_sel_hi:[0,0,0]
	v_mfma_scale_f32_16x16x128_f8f6f4 v[100:103], v[0:7], v[218:225], v[100:103], v191, v191 op_sel_hi:[0,0,0]
	v_mfma_scale_f32_16x16x128_f8f6f4 v[96:99], v[8:15], v[218:225], v[96:99], v191, v191 op_sel_hi:[0,0,0]
	s_barrier
	s_add_u32 s26, s26, 0x20080
	s_addc_u32 s27, s27, 0
	s_mov_b32 m0, s1
	v_lshl_add_u64 v[0:1], s[26:27], 0, v[162:163]
	global_load_lds_dwordx4 v[0:1], off
	v_lshl_add_u64 v[0:1], s[26:27], 0, v[164:165]
	s_mov_b32 m0, s56
	s_nop 0
	global_load_lds_dwordx4 v[0:1], off
	s_waitcnt vmcnt(6)
	s_barrier
	v_mfma_scale_f32_16x16x128_f8f6f4 v[60:63], v[234:241], v[16:23], v[60:63], v191, v191 op_sel_hi:[0,0,0]
	v_mfma_scale_f32_16x16x128_f8f6f4 v[56:59], v[242:249], v[16:23], v[56:59], v191, v191 op_sel_hi:[0,0,0]
	v_mfma_scale_f32_16x16x128_f8f6f4 v[52:55], v[234:241], v[24:31], v[52:55], v191, v191 op_sel_hi:[0,0,0]
	v_mfma_scale_f32_16x16x128_f8f6f4 v[48:51], v[242:249], v[24:31], v[48:51], v191, v191 op_sel_hi:[0,0,0]
	v_mfma_scale_f32_16x16x128_f8f6f4 v[44:47], v[234:241], v[178:185], v[44:47], v191, v191 op_sel_hi:[0,0,0]
	v_mfma_scale_f32_16x16x128_f8f6f4 v[40:43], v[242:249], v[178:185], v[40:43], v191, v191 op_sel_hi:[0,0,0]
	v_mfma_scale_f32_16x16x128_f8f6f4 v[36:39], v[234:241], v[218:225], v[36:39], v191, v191 op_sel_hi:[0,0,0]
	v_mfma_scale_f32_16x16x128_f8f6f4 v[32:35], v[242:249], v[218:225], v[32:35], v191, v191 op_sel_hi:[0,0,0]
	s_add_i32 s13, s13, 2
	s_add_u32 s24, s24, 0x100
	s_addc_u32 s25, s25, 0
	s_add_u32 s2, s2, 0x100
	s_addc_u32 s3, s3, 0
	s_cmp_gt_u32 s13, 5
	s_barrier
	s_cbranch_scc1 .LBB0_541

.LBB0_1319:
	ds_read_b128 v[142:145], v186
	ds_read_b128 v[146:149], v186 offset:1024
	ds_read_b128 v[150:153], v186 offset:2048
	ds_read_b128 v[162:165], v186 offset:3072
	s_add_u32 s30, s26, 0x80
	s_addc_u32 s31, s27, 0
	s_and_b64 s[28:29], s[28:29], exec
	s_cselect_b32 s31, s19, s31
	s_cselect_b32 s30, s18, s30
	s_cselect_b32 s29, s17, s15
	s_cselect_b32 s28, s16, s9
	v_lshl_add_u64 v[154:155], s[26:27], 0, v[128:129]
	s_add_i32 m0, s23, 0xc000
	ds_read_b128 v[166:169], v185
	ds_read_b128 v[174:177], v185 offset:1024
	ds_read_b128 v[178:181], v185 offset:2048
	ds_read_b128 v[204:207], v185 offset:3072
	ds_read_b128 v[208:211], v185 offset:4096
	ds_read_b128 v[214:217], v185 offset:5120
	ds_read_b128 v[218:221], v185 offset:6144
	ds_read_b128 v[222:225], v185 offset:7168
	global_load_lds_dwordx4 v[154:155], off
	v_lshl_add_u64 v[154:155], s[26:27], 0, v[132:133]
	s_add_i32 m0, s23, 0xe000
	s_nop 0
	global_load_lds_dwordx4 v[154:155], off
	s_waitcnt lgkmcnt(8)
	s_barrier
	s_waitcnt lgkmcnt(0)
	s_waitcnt lgkmcnt(0)
	v_mfma_f32_16x16x32_bf16 v[124:127], v[142:145], v[166:169], v[124:127]
	v_mfma_f32_16x16x32_bf16 v[120:123], v[150:153], v[166:169], v[120:123]
	v_mfma_f32_16x16x32_bf16 v[116:119], v[142:145], v[178:181], v[116:119]
	v_mfma_f32_16x16x32_bf16 v[112:115], v[150:153], v[178:181], v[112:115]
	v_mfma_f32_16x16x32_bf16 v[108:111], v[142:145], v[208:211], v[108:111]
	v_mfma_f32_16x16x32_bf16 v[104:107], v[150:153], v[208:211], v[104:107]
	v_mfma_f32_16x16x32_bf16 v[100:103], v[142:145], v[218:221], v[100:103]
	v_mfma_f32_16x16x32_bf16 v[96:99], v[150:153], v[218:221], v[96:99]
	v_mfma_f32_16x16x32_bf16 v[124:127], v[146:149], v[174:177], v[124:127]
	v_mfma_f32_16x16x32_bf16 v[120:123], v[162:165], v[174:177], v[120:123]
	v_mfma_f32_16x16x32_bf16 v[116:119], v[146:149], v[204:207], v[116:119]
	v_mfma_f32_16x16x32_bf16 v[112:115], v[162:165], v[204:207], v[112:115]
	v_mfma_f32_16x16x32_bf16 v[108:111], v[146:149], v[214:217], v[108:111]
	v_mfma_f32_16x16x32_bf16 v[104:107], v[162:165], v[214:217], v[104:107]
	v_mfma_f32_16x16x32_bf16 v[100:103], v[146:149], v[222:225], v[100:103]
	v_mfma_f32_16x16x32_bf16 v[96:99], v[162:165], v[222:225], v[96:99]
	s_barrier
	s_mov_b32 m0, s25
	v_lshl_add_u64 v[170:171], s[28:29], 0, v[158:159]
	ds_read_b128 v[226:229], v186 offset:16384
	ds_read_b128 v[230:233], v186 offset:17408
	ds_read_b128 v[234:237], v186 offset:18432
	ds_read_b128 v[238:241], v186 offset:19456
	global_load_lds_dwordx4 v[170:171], off
	v_lshl_add_u64 v[182:183], s[28:29], 0, v[160:161]
	s_mov_b32 m0, s51
	s_nop 0
	global_load_lds_dwordx4 v[182:183], off
	s_barrier
	s_waitcnt lgkmcnt(0)
	s_waitcnt lgkmcnt(0)
	v_mfma_f32_16x16x32_bf16 v[68:71], v[226:229], v[166:169], v[68:71]
	v_mfma_f32_16x16x32_bf16 v[64:67], v[234:237], v[166:169], v[64:67]
	v_mfma_f32_16x16x32_bf16 v[52:55], v[226:229], v[178:181], v[52:55]
	v_mfma_f32_16x16x32_bf16 v[48:51], v[234:237], v[178:181], v[48:51]
	v_mfma_f32_16x16x32_bf16 v[44:47], v[226:229], v[208:211], v[44:47]
	v_mfma_f32_16x16x32_bf16 v[40:43], v[234:237], v[208:211], v[40:43]
	v_mfma_f32_16x16x32_bf16 v[36:39], v[226:229], v[218:221], v[36:39]
	v_mfma_f32_16x16x32_bf16 v[32:35], v[234:237], v[218:221], v[32:35]
	v_mfma_f32_16x16x32_bf16 v[68:71], v[230:233], v[174:177], v[68:71]
	v_mfma_f32_16x16x32_bf16 v[64:67], v[238:241], v[174:177], v[64:67]
	v_mfma_f32_16x16x32_bf16 v[52:55], v[230:233], v[204:207], v[52:55]
	v_mfma_f32_16x16x32_bf16 v[48:51], v[238:241], v[204:207], v[48:51]
	v_mfma_f32_16x16x32_bf16 v[44:47], v[230:233], v[214:217], v[44:47]
	v_mfma_f32_16x16x32_bf16 v[40:43], v[238:241], v[214:217], v[40:43]
	v_mfma_f32_16x16x32_bf16 v[36:39], v[230:233], v[222:225], v[36:39]
	v_mfma_f32_16x16x32_bf16 v[32:35], v[238:241], v[222:225], v[32:35]
	s_mov_b32 m0, s23
	s_barrier
	ds_read_b128 v[166:169], v185 offset:16384
	ds_read_b128 v[174:177], v185 offset:17408
	ds_read_b128 v[178:181], v185 offset:18432
	ds_read_b128 v[204:207], v185 offset:19456
	ds_read_b128 v[208:211], v185 offset:20480
	ds_read_b128 v[214:217], v185 offset:21504
	ds_read_b128 v[218:221], v185 offset:22528
	ds_read_b128 v[222:225], v185 offset:23552
	global_load_lds_dwordx4 v172, s[30:31]
	s_mov_b32 m0, s56
	v_mov_b32_e32 v141, v173
	global_load_lds_dwordx4 v140, s[30:31]
	s_barrier
	s_waitcnt lgkmcnt(0)
	v_lshl_add_u64 v[196:197], s[30:31], 0, v[172:173]
	v_lshl_add_u64 v[242:243], s[30:31], 0, v[140:141]
	s_waitcnt lgkmcnt(0)
	v_mfma_f32_16x16x32_bf16 v[92:95], v[142:145], v[166:169], v[92:95]
	v_mfma_f32_16x16x32_bf16 v[88:91], v[150:153], v[166:169], v[88:91]
	v_mfma_f32_16x16x32_bf16 v[84:87], v[142:145], v[178:181], v[84:87]
	v_mfma_f32_16x16x32_bf16 v[80:83], v[150:153], v[178:181], v[80:83]
	v_mfma_f32_16x16x32_bf16 v[76:79], v[142:145], v[208:211], v[76:79]
	v_mfma_f32_16x16x32_bf16 v[72:75], v[150:153], v[208:211], v[72:75]
	v_mfma_f32_16x16x32_bf16 v[60:63], v[142:145], v[218:221], v[60:63]
	v_mfma_f32_16x16x32_bf16 v[56:59], v[150:153], v[218:221], v[56:59]
	v_mfma_f32_16x16x32_bf16 v[92:95], v[146:149], v[174:177], v[92:95]
	v_mfma_f32_16x16x32_bf16 v[88:91], v[162:165], v[174:177], v[88:91]
	v_mfma_f32_16x16x32_bf16 v[84:87], v[146:149], v[204:207], v[84:87]
	v_mfma_f32_16x16x32_bf16 v[80:83], v[162:165], v[204:207], v[80:83]
	v_mfma_f32_16x16x32_bf16 v[76:79], v[146:149], v[214:217], v[76:79]
	v_mfma_f32_16x16x32_bf16 v[72:75], v[162:165], v[214:217], v[72:75]
	v_mfma_f32_16x16x32_bf16 v[60:63], v[146:149], v[222:225], v[60:63]
	v_mfma_f32_16x16x32_bf16 v[56:59], v[162:165], v[222:225], v[56:59]
	s_barrier
	s_add_u32 s94, s28, 0x40000
	s_addc_u32 s95, s29, 0
	s_mov_b32 m0, s65
	v_lshl_add_u64 v[140:141], s[94:95], 0, v[158:159]
	global_load_lds_dwordx4 v[140:141], off
	v_lshl_add_u64 v[140:141], s[94:95], 0, v[160:161]
	s_mov_b32 m0, s70
	s_nop 0
	global_load_lds_dwordx4 v[140:141], off
	s_waitcnt vmcnt(6)
	s_barrier
	v_mfma_f32_16x16x32_bf16 v[28:31], v[226:229], v[166:169], v[28:31]
	v_mfma_f32_16x16x32_bf16 v[24:27], v[234:237], v[166:169], v[24:27]
	v_mfma_f32_16x16x32_bf16 v[20:23], v[226:229], v[178:181], v[20:23]
	v_mfma_f32_16x16x32_bf16 v[16:19], v[234:237], v[178:181], v[16:19]
	v_mfma_f32_16x16x32_bf16 v[12:15], v[226:229], v[208:211], v[12:15]
	v_mfma_f32_16x16x32_bf16 v[8:11], v[234:237], v[208:211], v[8:11]
	v_mfma_f32_16x16x32_bf16 v[4:7], v[226:229], v[218:221], v[4:7]
	v_mfma_f32_16x16x32_bf16 v[0:3], v[234:237], v[218:221], v[0:3]
	v_mfma_f32_16x16x32_bf16 v[28:31], v[230:233], v[174:177], v[28:31]
	v_mfma_f32_16x16x32_bf16 v[24:27], v[238:241], v[174:177], v[24:27]
	v_mfma_f32_16x16x32_bf16 v[20:23], v[230:233], v[204:207], v[20:23]
	v_mfma_f32_16x16x32_bf16 v[16:19], v[238:241], v[204:207], v[16:19]
	v_mfma_f32_16x16x32_bf16 v[12:15], v[230:233], v[214:217], v[12:15]
	v_mfma_f32_16x16x32_bf16 v[8:11], v[238:241], v[214:217], v[8:11]
	v_mfma_f32_16x16x32_bf16 v[4:7], v[230:233], v[222:225], v[4:7]
	v_mfma_f32_16x16x32_bf16 v[0:3], v[238:241], v[222:225], v[0:3]
	s_barrier
	ds_read_b128 v[140:143], v186 offset:32768
	ds_read_b128 v[144:147], v186 offset:33792
	ds_read_b128 v[148:151], v186 offset:34816
	ds_read_b128 v[152:155], v186 offset:35840
	s_mov_b32 m0, s71
	v_lshl_add_u64 v[138:139], s[30:31], 0, v[138:139]
	ds_read_b128 v[162:165], v185 offset:32768
	ds_read_b128 v[166:169], v185 offset:33792
	ds_read_b128 v[174:177], v185 offset:34816
	ds_read_b128 v[178:181], v185 offset:35840
	ds_read_b128 v[204:207], v185 offset:36864
	ds_read_b128 v[208:211], v185 offset:37888
	ds_read_b128 v[214:217], v185 offset:38912
	ds_read_b128 v[218:221], v185 offset:39936
	global_load_lds_dwordx4 v[138:139], off
	v_lshl_add_u64 v[136:137], s[30:31], 0, v[136:137]
	s_mov_b32 m0, s80
	s_nop 0
	global_load_lds_dwordx4 v[136:137], off
	s_waitcnt lgkmcnt(8)
	s_barrier
	s_waitcnt lgkmcnt(0)
	s_waitcnt lgkmcnt(0)
	v_mfma_f32_16x16x32_bf16 v[124:127], v[140:143], v[162:165], v[124:127]
	v_mfma_f32_16x16x32_bf16 v[120:123], v[148:151], v[162:165], v[120:123]
	v_mfma_f32_16x16x32_bf16 v[116:119], v[140:143], v[174:177], v[116:119]
	v_mfma_f32_16x16x32_bf16 v[112:115], v[148:151], v[174:177], v[112:115]
	v_mfma_f32_16x16x32_bf16 v[108:111], v[140:143], v[204:207], v[108:111]
	v_mfma_f32_16x16x32_bf16 v[104:107], v[148:151], v[204:207], v[104:107]
	v_mfma_f32_16x16x32_bf16 v[100:103], v[140:143], v[214:217], v[100:103]
	v_mfma_f32_16x16x32_bf16 v[96:99], v[148:151], v[214:217], v[96:99]
	v_mfma_f32_16x16x32_bf16 v[124:127], v[144:147], v[166:169], v[124:127]
	v_mfma_f32_16x16x32_bf16 v[120:123], v[152:155], v[166:169], v[120:123]
	v_mfma_f32_16x16x32_bf16 v[116:119], v[144:147], v[178:181], v[116:119]
	v_mfma_f32_16x16x32_bf16 v[112:115], v[152:155], v[178:181], v[112:115]
	v_mfma_f32_16x16x32_bf16 v[108:111], v[144:147], v[208:211], v[108:111]
	v_mfma_f32_16x16x32_bf16 v[104:107], v[152:155], v[208:211], v[104:107]
	v_mfma_f32_16x16x32_bf16 v[100:103], v[144:147], v[218:221], v[100:103]
	v_mfma_f32_16x16x32_bf16 v[96:99], v[152:155], v[218:221], v[96:99]
	s_barrier
	s_mov_b32 m0, s81
	v_lshl_add_u64 v[170:171], v[170:171], 0, s[40:41]
	ds_read_b128 v[136:139], v186 offset:49152
	ds_read_b128 v[222:225], v186 offset:50176
	ds_read_b128 v[226:229], v186 offset:51200
	ds_read_b128 v[230:233], v186 offset:52224
	global_load_lds_dwordx4 v[170:171], off
	v_lshl_add_u64 v[170:171], v[182:183], 0, s[40:41]
	s_mov_b32 m0, s82
	s_nop 0
	global_load_lds_dwordx4 v[170:171], off
	s_barrier
	s_waitcnt lgkmcnt(0)
	s_waitcnt lgkmcnt(0)
	v_mfma_f32_16x16x32_bf16 v[68:71], v[136:139], v[162:165], v[68:71]
	v_mfma_f32_16x16x32_bf16 v[64:67], v[226:229], v[162:165], v[64:67]
	v_mfma_f32_16x16x32_bf16 v[52:55], v[136:139], v[174:177], v[52:55]
	v_mfma_f32_16x16x32_bf16 v[48:51], v[226:229], v[174:177], v[48:51]
	v_mfma_f32_16x16x32_bf16 v[44:47], v[136:139], v[204:207], v[44:47]
	v_mfma_f32_16x16x32_bf16 v[40:43], v[226:229], v[204:207], v[40:43]
	v_mfma_f32_16x16x32_bf16 v[36:39], v[136:139], v[214:217], v[36:39]
	v_mfma_f32_16x16x32_bf16 v[32:35], v[226:229], v[214:217], v[32:35]
	v_mfma_f32_16x16x32_bf16 v[68:71], v[222:225], v[166:169], v[68:71]
	v_mfma_f32_16x16x32_bf16 v[64:67], v[230:233], v[166:169], v[64:67]
	v_mfma_f32_16x16x32_bf16 v[52:55], v[222:225], v[178:181], v[52:55]
	v_mfma_f32_16x16x32_bf16 v[48:51], v[230:233], v[178:181], v[48:51]
	v_mfma_f32_16x16x32_bf16 v[44:47], v[222:225], v[208:211], v[44:47]
	v_mfma_f32_16x16x32_bf16 v[40:43], v[230:233], v[208:211], v[40:43]
	v_mfma_f32_16x16x32_bf16 v[36:39], v[222:225], v[218:221], v[36:39]
	v_mfma_f32_16x16x32_bf16 v[32:35], v[230:233], v[218:221], v[32:35]
	s_mov_b32 m0, s83
	v_lshl_add_u64 v[170:171], v[196:197], 0, s[40:41]
	s_barrier
	ds_read_b128 v[162:165], v185 offset:49152
	ds_read_b128 v[166:169], v185 offset:50176
	ds_read_b128 v[174:177], v185 offset:51200
	ds_read_b128 v[178:181], v185 offset:52224
	ds_read_b128 v[204:207], v185 offset:53248
	ds_read_b128 v[208:211], v185 offset:54272
	ds_read_b128 v[214:217], v185 offset:55296
	ds_read_b128 v[218:221], v185 offset:56320
	global_load_lds_dwordx4 v[170:171], off
	v_lshl_add_u64 v[170:171], v[242:243], 0, s[40:41]
	s_mov_b32 m0, s85
	s_nop 0
	global_load_lds_dwordx4 v[170:171], off
	s_barrier
	s_waitcnt lgkmcnt(0)
	s_waitcnt lgkmcnt(0)
	v_mfma_f32_16x16x32_bf16 v[92:95], v[140:143], v[162:165], v[92:95]
	v_mfma_f32_16x16x32_bf16 v[88:91], v[148:151], v[162:165], v[88:91]
	v_mfma_f32_16x16x32_bf16 v[84:87], v[140:143], v[174:177], v[84:87]
	v_mfma_f32_16x16x32_bf16 v[80:83], v[148:151], v[174:177], v[80:83]
	v_mfma_f32_16x16x32_bf16 v[76:79], v[140:143], v[204:207], v[76:79]
	v_mfma_f32_16x16x32_bf16 v[72:75], v[148:151], v[204:207], v[72:75]
	v_mfma_f32_16x16x32_bf16 v[60:63], v[140:143], v[214:217], v[60:63]
	v_mfma_f32_16x16x32_bf16 v[56:59], v[148:151], v[214:217], v[56:59]
	v_mfma_f32_16x16x32_bf16 v[92:95], v[144:147], v[166:169], v[92:95]
	v_mfma_f32_16x16x32_bf16 v[88:91], v[152:155], v[166:169], v[88:91]
	v_mfma_f32_16x16x32_bf16 v[84:87], v[144:147], v[178:181], v[84:87]
	v_mfma_f32_16x16x32_bf16 v[80:83], v[152:155], v[178:181], v[80:83]
	v_mfma_f32_16x16x32_bf16 v[76:79], v[144:147], v[208:211], v[76:79]
	v_mfma_f32_16x16x32_bf16 v[72:75], v[152:155], v[208:211], v[72:75]
	v_mfma_f32_16x16x32_bf16 v[60:63], v[144:147], v[218:221], v[60:63]
	v_mfma_f32_16x16x32_bf16 v[56:59], v[152:155], v[218:221], v[56:59]
	s_barrier
	s_add_u32 s28, s28, 0x40080
	s_addc_u32 s29, s29, 0
	s_mov_b32 m0, s87
	v_lshl_add_u64 v[140:141], s[28:29], 0, v[158:159]
	global_load_lds_dwordx4 v[140:141], off
	v_lshl_add_u64 v[140:141], s[28:29], 0, v[160:161]
	s_mov_b32 m0, s44
	s_nop 0
	global_load_lds_dwordx4 v[140:141], off
	s_waitcnt vmcnt(6)
	s_barrier
	v_mfma_f32_16x16x32_bf16 v[28:31], v[136:139], v[162:165], v[28:31]
	v_mfma_f32_16x16x32_bf16 v[24:27], v[226:229], v[162:165], v[24:27]
	v_mfma_f32_16x16x32_bf16 v[20:23], v[136:139], v[174:177], v[20:23]
	v_mfma_f32_16x16x32_bf16 v[16:19], v[226:229], v[174:177], v[16:19]
	v_mfma_f32_16x16x32_bf16 v[12:15], v[136:139], v[204:207], v[12:15]
	v_mfma_f32_16x16x32_bf16 v[8:11], v[226:229], v[204:207], v[8:11]
	v_mfma_f32_16x16x32_bf16 v[4:7], v[136:139], v[214:217], v[4:7]
	v_mfma_f32_16x16x32_bf16 v[0:3], v[226:229], v[214:217], v[0:3]
	v_mfma_f32_16x16x32_bf16 v[28:31], v[222:225], v[166:169], v[28:31]
	v_mfma_f32_16x16x32_bf16 v[24:27], v[230:233], v[166:169], v[24:27]
	v_mfma_f32_16x16x32_bf16 v[20:23], v[222:225], v[178:181], v[20:23]
	v_mfma_f32_16x16x32_bf16 v[16:19], v[230:233], v[178:181], v[16:19]
	v_mfma_f32_16x16x32_bf16 v[12:15], v[222:225], v[208:211], v[12:15]
	v_mfma_f32_16x16x32_bf16 v[8:11], v[230:233], v[208:211], v[8:11]
	v_mfma_f32_16x16x32_bf16 v[4:7], v[222:225], v[218:221], v[4:7]
	v_mfma_f32_16x16x32_bf16 v[0:3], v[230:233], v[218:221], v[0:3]
	s_add_i32 vcc_lo, vcc_lo, 2
	s_add_u32 s26, s26, 0x100
	s_addc_u32 s27, s27, 0
	s_add_u32 s9, s9, 0x100
	s_addc_u32 s15, s15, 0
	s_cmp_gt_u32 vcc_lo, 13
	s_barrier
	s_cbranch_scc1 .LBB0_1303

.LBB0_1555:
	ds_read_b128 v[0:3], v191
	ds_read_b128 v[8:11], v191 offset:2048
	ds_read_b128 v[4:7], v193
	ds_read_b128 v[12:15], v193 offset:2048
	s_add_u32 s26, s22, 0x80
	s_addc_u32 s27, s23, 0
	s_and_b64 s[24:25], s[24:25], exec
	s_cselect_b32 s27, s19, s27
	s_cselect_b32 s26, s18, s26
	s_cselect_b32 s25, s17, s3
	s_cselect_b32 s24, s16, s2
	v_lshl_add_u64 v[16:17], s[22:23], 0, v[168:169]
	s_add_i32 m0, s44, 0xc000
	ds_read_b128 v[226:229], v190
	ds_read_b128 v[234:237], v190 offset:2048
	ds_read_b128 v[230:233], v192
	ds_read_b128 v[238:241], v192 offset:2048
	ds_read_b128 v[242:245], v190 offset:4096
	ds_read_b128 v[204:207], v190 offset:6144
	ds_read_b128 v[246:249], v192 offset:4096
	ds_read_b128 v[208:211], v192 offset:6144
	global_load_lds_dwordx4 v[16:17], off
	v_lshl_add_u64 v[16:17], s[22:23], 0, v[174:175]
	s_add_i32 m0, s44, 0xe000
	s_nop 0
	global_load_lds_dwordx4 v[16:17], off
	s_waitcnt lgkmcnt(8)
	s_barrier
	s_waitcnt lgkmcnt(0)
	s_waitcnt lgkmcnt(0)
	v_mfma_scale_f32_16x16x128_f8f6f4 v[156:159], v[0:7], v[226:233], v[156:159], v189, v189 op_sel_hi:[0,0,0]
	v_mfma_scale_f32_16x16x128_f8f6f4 v[148:151], v[8:15], v[226:233], v[148:151], v189, v189 op_sel_hi:[0,0,0]
	v_mfma_scale_f32_16x16x128_f8f6f4 v[140:143], v[0:7], v[234:241], v[140:143], v189, v189 op_sel_hi:[0,0,0]
	v_mfma_scale_f32_16x16x128_f8f6f4 v[132:135], v[8:15], v[234:241], v[132:135], v189, v189 op_sel_hi:[0,0,0]
	v_mfma_scale_f32_16x16x128_f8f6f4 v[124:127], v[0:7], v[242:249], v[124:127], v189, v189 op_sel_hi:[0,0,0]
	v_mfma_scale_f32_16x16x128_f8f6f4 v[116:119], v[8:15], v[242:249], v[116:119], v189, v189 op_sel_hi:[0,0,0]
	v_mfma_scale_f32_16x16x128_f8f6f4 v[108:111], v[0:7], v[204:211], v[108:111], v189, v189 op_sel_hi:[0,0,0]
	v_mfma_scale_f32_16x16x128_f8f6f4 v[100:103], v[8:15], v[204:211], v[100:103], v189, v189 op_sel_hi:[0,0,0]
	s_barrier
	s_mov_b32 m0, s46
	v_lshl_add_u64 v[180:181], s[24:25], 0, v[160:161]
	ds_read_b128 v[16:19], v191 offset:16384
	ds_read_b128 v[24:27], v191 offset:18432
	ds_read_b128 v[20:23], v193 offset:16384
	ds_read_b128 v[28:31], v193 offset:18432
	global_load_lds_dwordx4 v[180:181], off
	v_lshl_add_u64 v[182:183], s[24:25], 0, v[162:163]
	s_mov_b32 m0, s47
	s_nop 0
	global_load_lds_dwordx4 v[182:183], off
	s_barrier
	s_waitcnt lgkmcnt(0)
	s_waitcnt lgkmcnt(0)
	v_mfma_scale_f32_16x16x128_f8f6f4 v[152:155], v[16:23], v[226:233], v[152:155], v189, v189 op_sel_hi:[0,0,0]
	v_mfma_scale_f32_16x16x128_f8f6f4 v[144:147], v[24:31], v[226:233], v[144:147], v189, v189 op_sel_hi:[0,0,0]
	v_mfma_scale_f32_16x16x128_f8f6f4 v[136:139], v[16:23], v[234:241], v[136:139], v189, v189 op_sel_hi:[0,0,0]
	v_mfma_scale_f32_16x16x128_f8f6f4 v[128:131], v[24:31], v[234:241], v[128:131], v189, v189 op_sel_hi:[0,0,0]
	v_mfma_scale_f32_16x16x128_f8f6f4 v[120:123], v[16:23], v[242:249], v[120:123], v189, v189 op_sel_hi:[0,0,0]
	v_mfma_scale_f32_16x16x128_f8f6f4 v[112:115], v[24:31], v[242:249], v[112:115], v189, v189 op_sel_hi:[0,0,0]
	v_mfma_scale_f32_16x16x128_f8f6f4 v[104:107], v[16:23], v[204:211], v[104:107], v189, v189 op_sel_hi:[0,0,0]
	v_mfma_scale_f32_16x16x128_f8f6f4 v[96:99], v[24:31], v[204:211], v[96:99], v189, v189 op_sel_hi:[0,0,0]
	s_mov_b32 m0, s44
	s_barrier
	ds_read_b128 v[204:207], v190 offset:16384
	ds_read_b128 v[226:229], v190 offset:18432
	ds_read_b128 v[208:211], v192 offset:16384
	ds_read_b128 v[230:233], v192 offset:18432
	ds_read_b128 v[234:237], v190 offset:20480
	ds_read_b128 v[242:245], v190 offset:22528
	ds_read_b128 v[238:241], v192 offset:20480
	ds_read_b128 v[246:249], v192 offset:22528
	global_load_lds_dwordx4 v186, s[26:27]
	s_mov_b32 m0, s50
	v_mov_b32_e32 v187, v173
	global_load_lds_dwordx4 v184, s[26:27]
	s_barrier
	s_waitcnt lgkmcnt(0)
	v_mov_b32_e32 v185, v173
	v_lshl_add_u64 v[186:187], s[26:27], 0, v[186:187]
	v_lshl_add_u64 v[184:185], s[26:27], 0, v[184:185]
	s_waitcnt lgkmcnt(0)
	v_mfma_scale_f32_16x16x128_f8f6f4 v[92:95], v[0:7], v[204:211], v[92:95], v189, v189 op_sel_hi:[0,0,0]
	v_mfma_scale_f32_16x16x128_f8f6f4 v[84:87], v[8:15], v[204:211], v[84:87], v189, v189 op_sel_hi:[0,0,0]
	v_mfma_scale_f32_16x16x128_f8f6f4 v[76:79], v[0:7], v[226:233], v[76:79], v189, v189 op_sel_hi:[0,0,0]
	v_mfma_scale_f32_16x16x128_f8f6f4 v[68:71], v[8:15], v[226:233], v[68:71], v189, v189 op_sel_hi:[0,0,0]
	v_mfma_scale_f32_16x16x128_f8f6f4 v[60:63], v[0:7], v[234:241], v[60:63], v189, v189 op_sel_hi:[0,0,0]
	v_mfma_scale_f32_16x16x128_f8f6f4 v[52:55], v[8:15], v[234:241], v[52:55], v189, v189 op_sel_hi:[0,0,0]
	v_mfma_scale_f32_16x16x128_f8f6f4 v[44:47], v[0:7], v[242:249], v[44:47], v189, v189 op_sel_hi:[0,0,0]
	v_mfma_scale_f32_16x16x128_f8f6f4 v[36:39], v[8:15], v[242:249], v[36:39], v189, v189 op_sel_hi:[0,0,0]
	s_barrier
	s_add_u32 s72, s24, 0x20000
	s_addc_u32 s73, s25, 0
	s_mov_b32 m0, s51
	v_lshl_add_u64 v[0:1], s[72:73], 0, v[160:161]
	global_load_lds_dwordx4 v[0:1], off
	v_lshl_add_u64 v[0:1], s[72:73], 0, v[162:163]
	s_mov_b32 m0, s56
	s_nop 0
	global_load_lds_dwordx4 v[0:1], off
	s_waitcnt vmcnt(6)
	s_barrier
	v_mfma_scale_f32_16x16x128_f8f6f4 v[88:91], v[16:23], v[204:211], v[88:91], v189, v189 op_sel_hi:[0,0,0]
	v_mfma_scale_f32_16x16x128_f8f6f4 v[80:83], v[24:31], v[204:211], v[80:83], v189, v189 op_sel_hi:[0,0,0]
	v_mfma_scale_f32_16x16x128_f8f6f4 v[72:75], v[16:23], v[226:233], v[72:75], v189, v189 op_sel_hi:[0,0,0]
	v_mfma_scale_f32_16x16x128_f8f6f4 v[64:67], v[24:31], v[226:233], v[64:67], v189, v189 op_sel_hi:[0,0,0]
	v_mfma_scale_f32_16x16x128_f8f6f4 v[56:59], v[16:23], v[234:241], v[56:59], v189, v189 op_sel_hi:[0,0,0]
	v_mfma_scale_f32_16x16x128_f8f6f4 v[48:51], v[24:31], v[234:241], v[48:51], v189, v189 op_sel_hi:[0,0,0]
	v_mfma_scale_f32_16x16x128_f8f6f4 v[40:43], v[16:23], v[242:249], v[40:43], v189, v189 op_sel_hi:[0,0,0]
	v_mfma_scale_f32_16x16x128_f8f6f4 v[32:35], v[24:31], v[242:249], v[32:35], v189, v189 op_sel_hi:[0,0,0]
	s_barrier
	ds_read_b128 v[0:3], v191 offset:32768
	ds_read_b128 v[8:11], v191 offset:34816
	ds_read_b128 v[4:7], v193 offset:32768
	ds_read_b128 v[12:15], v193 offset:34816
	s_mov_b32 m0, s65
	v_lshl_add_u64 v[178:179], s[26:27], 0, v[178:179]
	ds_read_b128 v[16:19], v190 offset:32768
	ds_read_b128 v[24:27], v190 offset:34816
	ds_read_b128 v[20:23], v192 offset:32768
	ds_read_b128 v[28:31], v192 offset:34816
	ds_read_b128 v[204:207], v190 offset:36864
	ds_read_b128 v[226:229], v190 offset:38912
	ds_read_b128 v[208:211], v192 offset:36864
	ds_read_b128 v[230:233], v192 offset:38912
	global_load_lds_dwordx4 v[178:179], off
	v_lshl_add_u64 v[176:177], s[26:27], 0, v[176:177]
	s_mov_b32 m0, s70
	s_nop 0
	global_load_lds_dwordx4 v[176:177], off
	s_waitcnt lgkmcnt(8)
	s_barrier
	s_waitcnt lgkmcnt(0)
	s_waitcnt lgkmcnt(0)
	v_mfma_scale_f32_16x16x128_f8f6f4 v[156:159], v[0:7], v[16:23], v[156:159], v189, v189 op_sel_hi:[0,0,0]
	v_mfma_scale_f32_16x16x128_f8f6f4 v[148:151], v[8:15], v[16:23], v[148:151], v189, v189 op_sel_hi:[0,0,0]
	v_mfma_scale_f32_16x16x128_f8f6f4 v[140:143], v[0:7], v[24:31], v[140:143], v189, v189 op_sel_hi:[0,0,0]
	v_mfma_scale_f32_16x16x128_f8f6f4 v[132:135], v[8:15], v[24:31], v[132:135], v189, v189 op_sel_hi:[0,0,0]
	v_mfma_scale_f32_16x16x128_f8f6f4 v[124:127], v[0:7], v[204:211], v[124:127], v189, v189 op_sel_hi:[0,0,0]
	v_mfma_scale_f32_16x16x128_f8f6f4 v[116:119], v[8:15], v[204:211], v[116:119], v189, v189 op_sel_hi:[0,0,0]
	v_mfma_scale_f32_16x16x128_f8f6f4 v[108:111], v[0:7], v[226:233], v[108:111], v189, v189 op_sel_hi:[0,0,0]
	v_mfma_scale_f32_16x16x128_f8f6f4 v[100:103], v[8:15], v[226:233], v[100:103], v189, v189 op_sel_hi:[0,0,0]
	s_barrier
	s_mov_b32 m0, s71
	v_lshl_add_u64 v[176:177], v[180:181], 0, s[40:41]
	ds_read_b128 v[234:237], v191 offset:49152
	ds_read_b128 v[242:245], v191 offset:51200
	ds_read_b128 v[238:241], v193 offset:49152
	ds_read_b128 v[246:249], v193 offset:51200
	global_load_lds_dwordx4 v[176:177], off
	v_lshl_add_u64 v[176:177], v[182:183], 0, s[40:41]
	s_mov_b32 m0, s80
	s_nop 0
	global_load_lds_dwordx4 v[176:177], off
	s_barrier
	s_waitcnt lgkmcnt(0)
	s_waitcnt lgkmcnt(0)
	v_mfma_scale_f32_16x16x128_f8f6f4 v[152:155], v[234:241], v[16:23], v[152:155], v189, v189 op_sel_hi:[0,0,0]
	v_mfma_scale_f32_16x16x128_f8f6f4 v[144:147], v[242:249], v[16:23], v[144:147], v189, v189 op_sel_hi:[0,0,0]
	v_mfma_scale_f32_16x16x128_f8f6f4 v[136:139], v[234:241], v[24:31], v[136:139], v189, v189 op_sel_hi:[0,0,0]
	v_mfma_scale_f32_16x16x128_f8f6f4 v[128:131], v[242:249], v[24:31], v[128:131], v189, v189 op_sel_hi:[0,0,0]
	v_mfma_scale_f32_16x16x128_f8f6f4 v[120:123], v[234:241], v[204:211], v[120:123], v189, v189 op_sel_hi:[0,0,0]
	v_mfma_scale_f32_16x16x128_f8f6f4 v[112:115], v[242:249], v[204:211], v[112:115], v189, v189 op_sel_hi:[0,0,0]
	v_mfma_scale_f32_16x16x128_f8f6f4 v[104:107], v[234:241], v[226:233], v[104:107], v189, v189 op_sel_hi:[0,0,0]
	v_mfma_scale_f32_16x16x128_f8f6f4 v[96:99], v[242:249], v[226:233], v[96:99], v189, v189 op_sel_hi:[0,0,0]
	s_mov_b32 m0, s81
	v_lshl_add_u64 v[186:187], v[186:187], 0, s[40:41]
	s_barrier
	ds_read_b128 v[16:19], v190 offset:49152
	ds_read_b128 v[24:27], v190 offset:51200
	ds_read_b128 v[20:23], v192 offset:49152
	ds_read_b128 v[28:31], v192 offset:51200
	ds_read_b128 v[176:179], v190 offset:53248
	ds_read_b128 v[204:207], v190 offset:55296
	ds_read_b128 v[180:183], v192 offset:53248
	ds_read_b128 v[208:211], v192 offset:55296
	global_load_lds_dwordx4 v[186:187], off
	v_lshl_add_u64 v[184:185], v[184:185], 0, s[40:41]
	s_mov_b32 m0, s82
	s_nop 0
	global_load_lds_dwordx4 v[184:185], off
	s_barrier
	s_waitcnt lgkmcnt(0)
	s_waitcnt lgkmcnt(0)
	v_mfma_scale_f32_16x16x128_f8f6f4 v[92:95], v[0:7], v[16:23], v[92:95], v189, v189 op_sel_hi:[0,0,0]
	v_mfma_scale_f32_16x16x128_f8f6f4 v[84:87], v[8:15], v[16:23], v[84:87], v189, v189 op_sel_hi:[0,0,0]
	v_mfma_scale_f32_16x16x128_f8f6f4 v[76:79], v[0:7], v[24:31], v[76:79], v189, v189 op_sel_hi:[0,0,0]
	v_mfma_scale_f32_16x16x128_f8f6f4 v[68:71], v[8:15], v[24:31], v[68:71], v189, v189 op_sel_hi:[0,0,0]
	v_mfma_scale_f32_16x16x128_f8f6f4 v[60:63], v[0:7], v[176:183], v[60:63], v189, v189 op_sel_hi:[0,0,0]
	v_mfma_scale_f32_16x16x128_f8f6f4 v[52:55], v[8:15], v[176:183], v[52:55], v189, v189 op_sel_hi:[0,0,0]
	v_mfma_scale_f32_16x16x128_f8f6f4 v[44:47], v[0:7], v[204:211], v[44:47], v189, v189 op_sel_hi:[0,0,0]
	v_mfma_scale_f32_16x16x128_f8f6f4 v[36:39], v[8:15], v[204:211], v[36:39], v189, v189 op_sel_hi:[0,0,0]
	s_barrier
	s_add_u32 s24, s24, 0x20080
	s_addc_u32 s25, s25, 0
	s_mov_b32 m0, s83
	v_lshl_add_u64 v[0:1], s[24:25], 0, v[160:161]
	global_load_lds_dwordx4 v[0:1], off
	v_lshl_add_u64 v[0:1], s[24:25], 0, v[162:163]
	s_mov_b32 m0, s85
	s_nop 0
	global_load_lds_dwordx4 v[0:1], off
	s_waitcnt vmcnt(6)
	s_barrier
	v_mfma_scale_f32_16x16x128_f8f6f4 v[88:91], v[234:241], v[16:23], v[88:91], v189, v189 op_sel_hi:[0,0,0]
	v_mfma_scale_f32_16x16x128_f8f6f4 v[80:83], v[242:249], v[16:23], v[80:83], v189, v189 op_sel_hi:[0,0,0]
	v_mfma_scale_f32_16x16x128_f8f6f4 v[72:75], v[234:241], v[24:31], v[72:75], v189, v189 op_sel_hi:[0,0,0]
	v_mfma_scale_f32_16x16x128_f8f6f4 v[64:67], v[242:249], v[24:31], v[64:67], v189, v189 op_sel_hi:[0,0,0]
	v_mfma_scale_f32_16x16x128_f8f6f4 v[56:59], v[234:241], v[176:183], v[56:59], v189, v189 op_sel_hi:[0,0,0]
	v_mfma_scale_f32_16x16x128_f8f6f4 v[48:51], v[242:249], v[176:183], v[48:51], v189, v189 op_sel_hi:[0,0,0]
	v_mfma_scale_f32_16x16x128_f8f6f4 v[40:43], v[234:241], v[204:211], v[40:43], v189, v189 op_sel_hi:[0,0,0]
	v_mfma_scale_f32_16x16x128_f8f6f4 v[32:35], v[242:249], v[204:211], v[32:35], v189, v189 op_sel_hi:[0,0,0]
	s_add_i32 s64, s64, 2
	s_add_u32 s22, s22, 0x100
	s_addc_u32 s23, s23, 0
	s_add_u32 s2, s2, 0x100
	s_addc_u32 s3, s3, 0
	s_cmp_gt_u32 s64, 5
	s_barrier
	s_cbranch_scc1 .LBB0_1540

.LBB0_1666:
	ds_read_b128 v[0:3], v190
	ds_read_b128 v[8:11], v190 offset:2048
	ds_read_b128 v[4:7], v192
	ds_read_b128 v[12:15], v192 offset:2048
	s_add_u32 s26, s22, 0x80
	s_addc_u32 s27, s23, 0
	s_and_b64 s[24:25], s[24:25], exec
	s_cselect_b32 s27, s19, s27
	s_cselect_b32 s26, s18, s26
	s_cselect_b32 s25, s17, s83
	s_cselect_b32 s24, s16, s7
	v_lshl_add_u64 v[16:17], s[22:23], 0, v[166:167]
	s_add_i32 m0, s13, 0xc000
	ds_read_b128 v[204:207], v189
	ds_read_b128 v[216:219], v189 offset:2048
	ds_read_b128 v[208:211], v191
	ds_read_b128 v[220:223], v191 offset:2048
	ds_read_b128 v[224:227], v189 offset:4096
	ds_read_b128 v[232:235], v189 offset:6144
	ds_read_b128 v[228:231], v191 offset:4096
	ds_read_b128 v[236:239], v191 offset:6144
	global_load_lds_dwordx4 v[16:17], off
	v_lshl_add_u64 v[16:17], s[22:23], 0, v[170:171]
	s_add_i32 m0, s13, 0xe000
	s_nop 0
	global_load_lds_dwordx4 v[16:17], off
	s_waitcnt lgkmcnt(8)
	s_barrier
	s_waitcnt lgkmcnt(0)
	s_waitcnt lgkmcnt(0)
	v_mfma_scale_f32_16x16x128_f8f6f4 v[156:159], v[0:7], v[204:211], v[156:159], v188, v188 op_sel_hi:[0,0,0]
	v_mfma_scale_f32_16x16x128_f8f6f4 v[152:155], v[8:15], v[204:211], v[152:155], v188, v188 op_sel_hi:[0,0,0]
	v_mfma_scale_f32_16x16x128_f8f6f4 v[148:151], v[0:7], v[216:223], v[148:151], v188, v188 op_sel_hi:[0,0,0]
	v_mfma_scale_f32_16x16x128_f8f6f4 v[144:147], v[8:15], v[216:223], v[144:147], v188, v188 op_sel_hi:[0,0,0]
	v_mfma_scale_f32_16x16x128_f8f6f4 v[140:143], v[0:7], v[224:231], v[140:143], v188, v188 op_sel_hi:[0,0,0]
	v_mfma_scale_f32_16x16x128_f8f6f4 v[136:139], v[8:15], v[224:231], v[136:139], v188, v188 op_sel_hi:[0,0,0]
	v_mfma_scale_f32_16x16x128_f8f6f4 v[132:135], v[0:7], v[232:239], v[132:135], v188, v188 op_sel_hi:[0,0,0]
	v_mfma_scale_f32_16x16x128_f8f6f4 v[128:131], v[8:15], v[232:239], v[128:131], v188, v188 op_sel_hi:[0,0,0]
	s_barrier
	s_mov_b32 m0, s15
	v_lshl_add_u64 v[180:181], s[24:25], 0, v[162:163]
	ds_read_b128 v[16:19], v190 offset:16384
	ds_read_b128 v[24:27], v190 offset:18432
	ds_read_b128 v[20:23], v192 offset:16384
	ds_read_b128 v[28:31], v192 offset:18432
	global_load_lds_dwordx4 v[180:181], off
	v_lshl_add_u64 v[182:183], s[24:25], 0, v[164:165]
	s_mov_b32 m0, s31
	s_nop 0
	global_load_lds_dwordx4 v[182:183], off
	s_barrier
	s_waitcnt lgkmcnt(0)
	s_waitcnt lgkmcnt(0)
	v_mfma_scale_f32_16x16x128_f8f6f4 v[100:103], v[16:23], v[204:211], v[100:103], v188, v188 op_sel_hi:[0,0,0]
	v_mfma_scale_f32_16x16x128_f8f6f4 v[96:99], v[24:31], v[204:211], v[96:99], v188, v188 op_sel_hi:[0,0,0]
	v_mfma_scale_f32_16x16x128_f8f6f4 v[84:87], v[16:23], v[216:223], v[84:87], v188, v188 op_sel_hi:[0,0,0]
	v_mfma_scale_f32_16x16x128_f8f6f4 v[80:83], v[24:31], v[216:223], v[80:83], v188, v188 op_sel_hi:[0,0,0]
	v_mfma_scale_f32_16x16x128_f8f6f4 v[76:79], v[16:23], v[224:231], v[76:79], v188, v188 op_sel_hi:[0,0,0]
	v_mfma_scale_f32_16x16x128_f8f6f4 v[72:75], v[24:31], v[224:231], v[72:75], v188, v188 op_sel_hi:[0,0,0]
	v_mfma_scale_f32_16x16x128_f8f6f4 v[68:71], v[16:23], v[232:239], v[68:71], v188, v188 op_sel_hi:[0,0,0]
	v_mfma_scale_f32_16x16x128_f8f6f4 v[64:67], v[24:31], v[232:239], v[64:67], v188, v188 op_sel_hi:[0,0,0]
	s_mov_b32 m0, s13
	s_barrier
	ds_read_b128 v[204:207], v189 offset:16384
	ds_read_b128 v[216:219], v189 offset:18432
	ds_read_b128 v[208:211], v191 offset:16384
	ds_read_b128 v[220:223], v191 offset:18432
	ds_read_b128 v[224:227], v189 offset:20480
	ds_read_b128 v[232:235], v189 offset:22528
	ds_read_b128 v[228:231], v191 offset:20480
	ds_read_b128 v[236:239], v191 offset:22528
	global_load_lds_dwordx4 v172, s[26:27]
	s_mov_b32 m0, s44
	v_mov_b32_e32 v185, v173
	global_load_lds_dwordx4 v184, s[26:27]
	s_barrier
	s_waitcnt lgkmcnt(0)
	v_lshl_add_u64 v[186:187], s[26:27], 0, v[172:173]
	v_lshl_add_u64 v[184:185], s[26:27], 0, v[184:185]
	s_waitcnt lgkmcnt(0)
	v_mfma_scale_f32_16x16x128_f8f6f4 v[124:127], v[0:7], v[204:211], v[124:127], v188, v188 op_sel_hi:[0,0,0]
	v_mfma_scale_f32_16x16x128_f8f6f4 v[120:123], v[8:15], v[204:211], v[120:123], v188, v188 op_sel_hi:[0,0,0]
	v_mfma_scale_f32_16x16x128_f8f6f4 v[116:119], v[0:7], v[216:223], v[116:119], v188, v188 op_sel_hi:[0,0,0]
	v_mfma_scale_f32_16x16x128_f8f6f4 v[112:115], v[8:15], v[216:223], v[112:115], v188, v188 op_sel_hi:[0,0,0]
	v_mfma_scale_f32_16x16x128_f8f6f4 v[108:111], v[0:7], v[224:231], v[108:111], v188, v188 op_sel_hi:[0,0,0]
	v_mfma_scale_f32_16x16x128_f8f6f4 v[104:107], v[8:15], v[224:231], v[104:107], v188, v188 op_sel_hi:[0,0,0]
	v_mfma_scale_f32_16x16x128_f8f6f4 v[92:95], v[0:7], v[232:239], v[92:95], v188, v188 op_sel_hi:[0,0,0]
	v_mfma_scale_f32_16x16x128_f8f6f4 v[88:91], v[8:15], v[232:239], v[88:91], v188, v188 op_sel_hi:[0,0,0]
	s_barrier
	s_add_u32 s90, s24, 0x20000
	s_addc_u32 s91, s25, 0
	s_mov_b32 m0, s46
	v_lshl_add_u64 v[0:1], s[90:91], 0, v[162:163]
	global_load_lds_dwordx4 v[0:1], off
	v_lshl_add_u64 v[0:1], s[90:91], 0, v[164:165]
	s_mov_b32 m0, s47
	s_nop 0
	global_load_lds_dwordx4 v[0:1], off
	s_waitcnt vmcnt(6)
	s_barrier
	v_mfma_scale_f32_16x16x128_f8f6f4 v[60:63], v[16:23], v[204:211], v[60:63], v188, v188 op_sel_hi:[0,0,0]
	v_mfma_scale_f32_16x16x128_f8f6f4 v[56:59], v[24:31], v[204:211], v[56:59], v188, v188 op_sel_hi:[0,0,0]
	v_mfma_scale_f32_16x16x128_f8f6f4 v[52:55], v[16:23], v[216:223], v[52:55], v188, v188 op_sel_hi:[0,0,0]
	v_mfma_scale_f32_16x16x128_f8f6f4 v[48:51], v[24:31], v[216:223], v[48:51], v188, v188 op_sel_hi:[0,0,0]
	v_mfma_scale_f32_16x16x128_f8f6f4 v[44:47], v[16:23], v[224:231], v[44:47], v188, v188 op_sel_hi:[0,0,0]
	v_mfma_scale_f32_16x16x128_f8f6f4 v[40:43], v[24:31], v[224:231], v[40:43], v188, v188 op_sel_hi:[0,0,0]
	v_mfma_scale_f32_16x16x128_f8f6f4 v[36:39], v[16:23], v[232:239], v[36:39], v188, v188 op_sel_hi:[0,0,0]
	v_mfma_scale_f32_16x16x128_f8f6f4 v[32:35], v[24:31], v[232:239], v[32:35], v188, v188 op_sel_hi:[0,0,0]
	s_barrier
	ds_read_b128 v[0:3], v190 offset:32768
	ds_read_b128 v[8:11], v190 offset:34816
	ds_read_b128 v[4:7], v192 offset:32768
	ds_read_b128 v[12:15], v192 offset:34816
	s_mov_b32 m0, s50
	v_lshl_add_u64 v[178:179], s[26:27], 0, v[178:179]
	ds_read_b128 v[16:19], v189 offset:32768
	ds_read_b128 v[24:27], v189 offset:34816
	ds_read_b128 v[20:23], v191 offset:32768
	ds_read_b128 v[28:31], v191 offset:34816
	ds_read_b128 v[204:207], v189 offset:36864
	ds_read_b128 v[216:219], v189 offset:38912
	ds_read_b128 v[208:211], v191 offset:36864
	ds_read_b128 v[220:223], v191 offset:38912
	global_load_lds_dwordx4 v[178:179], off
	v_lshl_add_u64 v[176:177], s[26:27], 0, v[176:177]
	s_mov_b32 m0, s51
	s_nop 0
	global_load_lds_dwordx4 v[176:177], off
	s_waitcnt lgkmcnt(8)
	s_barrier
	s_waitcnt lgkmcnt(0)
	s_waitcnt lgkmcnt(0)
	v_mfma_scale_f32_16x16x128_f8f6f4 v[156:159], v[0:7], v[16:23], v[156:159], v188, v188 op_sel_hi:[0,0,0]
	v_mfma_scale_f32_16x16x128_f8f6f4 v[152:155], v[8:15], v[16:23], v[152:155], v188, v188 op_sel_hi:[0,0,0]
	v_mfma_scale_f32_16x16x128_f8f6f4 v[148:151], v[0:7], v[24:31], v[148:151], v188, v188 op_sel_hi:[0,0,0]
	v_mfma_scale_f32_16x16x128_f8f6f4 v[144:147], v[8:15], v[24:31], v[144:147], v188, v188 op_sel_hi:[0,0,0]
	v_mfma_scale_f32_16x16x128_f8f6f4 v[140:143], v[0:7], v[204:211], v[140:143], v188, v188 op_sel_hi:[0,0,0]
	v_mfma_scale_f32_16x16x128_f8f6f4 v[136:139], v[8:15], v[204:211], v[136:139], v188, v188 op_sel_hi:[0,0,0]
	v_mfma_scale_f32_16x16x128_f8f6f4 v[132:135], v[0:7], v[216:223], v[132:135], v188, v188 op_sel_hi:[0,0,0]
	v_mfma_scale_f32_16x16x128_f8f6f4 v[128:131], v[8:15], v[216:223], v[128:131], v188, v188 op_sel_hi:[0,0,0]
	s_barrier
	s_mov_b32 m0, s56
	v_lshl_add_u64 v[176:177], v[180:181], 0, s[40:41]
	ds_read_b128 v[224:227], v190 offset:49152
	ds_read_b128 v[232:235], v190 offset:51200
	ds_read_b128 v[228:231], v192 offset:49152
	ds_read_b128 v[236:239], v192 offset:51200
	global_load_lds_dwordx4 v[176:177], off
	v_lshl_add_u64 v[176:177], v[182:183], 0, s[40:41]
	s_mov_b32 m0, s57
	s_nop 0
	global_load_lds_dwordx4 v[176:177], off
	s_barrier
	s_waitcnt lgkmcnt(0)
	s_waitcnt lgkmcnt(0)
	v_mfma_scale_f32_16x16x128_f8f6f4 v[100:103], v[224:231], v[16:23], v[100:103], v188, v188 op_sel_hi:[0,0,0]
	v_mfma_scale_f32_16x16x128_f8f6f4 v[96:99], v[232:239], v[16:23], v[96:99], v188, v188 op_sel_hi:[0,0,0]
	v_mfma_scale_f32_16x16x128_f8f6f4 v[84:87], v[224:231], v[24:31], v[84:87], v188, v188 op_sel_hi:[0,0,0]
	v_mfma_scale_f32_16x16x128_f8f6f4 v[80:83], v[232:239], v[24:31], v[80:83], v188, v188 op_sel_hi:[0,0,0]
	v_mfma_scale_f32_16x16x128_f8f6f4 v[76:79], v[224:231], v[204:211], v[76:79], v188, v188 op_sel_hi:[0,0,0]
	v_mfma_scale_f32_16x16x128_f8f6f4 v[72:75], v[232:239], v[204:211], v[72:75], v188, v188 op_sel_hi:[0,0,0]
	v_mfma_scale_f32_16x16x128_f8f6f4 v[68:71], v[224:231], v[216:223], v[68:71], v188, v188 op_sel_hi:[0,0,0]
	v_mfma_scale_f32_16x16x128_f8f6f4 v[64:67], v[232:239], v[216:223], v[64:67], v188, v188 op_sel_hi:[0,0,0]
	s_mov_b32 m0, s64
	v_lshl_add_u64 v[186:187], v[186:187], 0, s[40:41]
	s_barrier
	ds_read_b128 v[16:19], v189 offset:49152
	ds_read_b128 v[24:27], v189 offset:51200
	ds_read_b128 v[20:23], v191 offset:49152
	ds_read_b128 v[28:31], v191 offset:51200
	ds_read_b128 v[176:179], v189 offset:53248
	ds_read_b128 v[204:207], v189 offset:55296
	ds_read_b128 v[180:183], v191 offset:53248
	ds_read_b128 v[208:211], v191 offset:55296
	global_load_lds_dwordx4 v[186:187], off
	v_lshl_add_u64 v[184:185], v[184:185], 0, s[40:41]
	s_mov_b32 m0, s65
	s_nop 0
	global_load_lds_dwordx4 v[184:185], off
	s_barrier
	s_waitcnt lgkmcnt(0)
	s_waitcnt lgkmcnt(0)
	v_mfma_scale_f32_16x16x128_f8f6f4 v[124:127], v[0:7], v[16:23], v[124:127], v188, v188 op_sel_hi:[0,0,0]
	v_mfma_scale_f32_16x16x128_f8f6f4 v[120:123], v[8:15], v[16:23], v[120:123], v188, v188 op_sel_hi:[0,0,0]
	v_mfma_scale_f32_16x16x128_f8f6f4 v[116:119], v[0:7], v[24:31], v[116:119], v188, v188 op_sel_hi:[0,0,0]
	v_mfma_scale_f32_16x16x128_f8f6f4 v[112:115], v[8:15], v[24:31], v[112:115], v188, v188 op_sel_hi:[0,0,0]
	v_mfma_scale_f32_16x16x128_f8f6f4 v[108:111], v[0:7], v[176:183], v[108:111], v188, v188 op_sel_hi:[0,0,0]
	v_mfma_scale_f32_16x16x128_f8f6f4 v[104:107], v[8:15], v[176:183], v[104:107], v188, v188 op_sel_hi:[0,0,0]
	v_mfma_scale_f32_16x16x128_f8f6f4 v[92:95], v[0:7], v[204:211], v[92:95], v188, v188 op_sel_hi:[0,0,0]
	v_mfma_scale_f32_16x16x128_f8f6f4 v[88:91], v[8:15], v[204:211], v[88:91], v188, v188 op_sel_hi:[0,0,0]
	s_barrier
	s_add_u32 s24, s24, 0x20080
	s_addc_u32 s25, s25, 0
	s_mov_b32 m0, s70
	v_lshl_add_u64 v[0:1], s[24:25], 0, v[162:163]
	global_load_lds_dwordx4 v[0:1], off
	v_lshl_add_u64 v[0:1], s[24:25], 0, v[164:165]
	s_mov_b32 m0, s71
	s_nop 0
	global_load_lds_dwordx4 v[0:1], off
	s_waitcnt vmcnt(6)
	s_barrier
	v_mfma_scale_f32_16x16x128_f8f6f4 v[60:63], v[224:231], v[16:23], v[60:63], v188, v188 op_sel_hi:[0,0,0]
	v_mfma_scale_f32_16x16x128_f8f6f4 v[56:59], v[232:239], v[16:23], v[56:59], v188, v188 op_sel_hi:[0,0,0]
	v_mfma_scale_f32_16x16x128_f8f6f4 v[52:55], v[224:231], v[24:31], v[52:55], v188, v188 op_sel_hi:[0,0,0]
	v_mfma_scale_f32_16x16x128_f8f6f4 v[48:51], v[232:239], v[24:31], v[48:51], v188, v188 op_sel_hi:[0,0,0]
	v_mfma_scale_f32_16x16x128_f8f6f4 v[44:47], v[224:231], v[176:183], v[44:47], v188, v188 op_sel_hi:[0,0,0]
	v_mfma_scale_f32_16x16x128_f8f6f4 v[40:43], v[232:239], v[176:183], v[40:43], v188, v188 op_sel_hi:[0,0,0]
	v_mfma_scale_f32_16x16x128_f8f6f4 v[36:39], v[224:231], v[204:211], v[36:39], v188, v188 op_sel_hi:[0,0,0]
	v_mfma_scale_f32_16x16x128_f8f6f4 v[32:35], v[232:239], v[204:211], v[32:35], v188, v188 op_sel_hi:[0,0,0]
	s_add_i32 s85, s85, 2
	s_add_u32 s22, s22, 0x100
	s_addc_u32 s23, s23, 0
	s_add_u32 s7, s7, 0x100
	s_addc_u32 s83, s83, 0
	s_cmp_gt_u32 s85, 5
	s_barrier
	s_cbranch_scc1 .LBB0_1655
